# grid barrier non-leader path: buffer_inv sc1 issued before polling the XCC generation word (overlaps the wait) instead of after release; on top of v5
# baseline (speedup 1.0000x reference)
.LBB0_170:
	s_lshl_b32 s8, s45, 8
	s_add_u32 s8, s2, s8
	s_addc_u32 s9, s3, 0
	v_mov_b32_e32 v1, 0x1000
	v_mov_b32_e32 v3, 1
	global_atomic_add v3, v1, v3, s[8:9] offset:1024 sc0
	v_cvt_f32_u32_e32 v1, v2
	v_sub_u32_e32 v4, 0, v2
	v_rcp_iflag_f32_e32 v1, v1
	s_nop 0
	v_mul_f32_e32 v1, 0x4f7ffffe, v1
	v_cvt_u32_f32_e32 v1, v1
	v_mul_lo_u32 v4, v4, v1
	v_mul_hi_u32 v4, v1, v4
	v_add_u32_e32 v1, v1, v4
	s_waitcnt vmcnt(0)
	v_mul_hi_u32 v1, v3, v1
	v_mul_lo_u32 v4, v1, v2
	v_sub_u32_e32 v4, v3, v4
	v_add_u32_e32 v5, 1, v1
	v_cmp_ge_u32_e32 vcc, v4, v2
	v_add_u32_e32 v3, 1, v3
	s_nop 0
	v_cndmask_b32_e32 v1, v1, v5, vcc
	v_sub_u32_e32 v5, v4, v2
	v_cndmask_b32_e32 v4, v4, v5, vcc
	v_add_u32_e32 v5, 1, v1
	v_cmp_ge_u32_e32 vcc, v4, v2
	s_nop 1
	v_cndmask_b32_e32 v1, v1, v5, vcc
	v_mul_lo_u32 v4, v2, v1
	v_add_u32_e32 v2, v4, v2
	v_cmp_ne_u32_e32 vcc, v3, v2
	s_and_saveexec_b64 s[10:11], vcc
	s_xor_b64 s[10:11], exec, s[10:11]
	s_cbranch_execz .LBB0_184
	s_waitcnt lgkmcnt(0)
	v_mov_b32_e32 v0, 0x2000
	buffer_inv sc1
	global_load_dword v0, v0, s[8:9] offset:1024 sc1
	s_add_u32 s16, s8, 0x2400
	s_addc_u32 s17, s9, 0
	s_waitcnt vmcnt(0)
	v_cmp_eq_u32_e32 vcc, v0, v1
	s_and_saveexec_b64 s[12:13], vcc
	s_cbranch_execz .LBB0_183
	s_load_dwordx2 s[14:15], s[0:1], 0xc8
	s_mov_b32 s28, 1
	s_mov_b64 s[18:19], 0
	v_mov_b32_e32 v0, 0
	s_waitcnt lgkmcnt(0)
	s_add_u32 s14, s14, 0x4200
	s_addc_u32 s15, s15, 0
	s_branch .LBB0_174

.LBB0_183:
	s_or_b64 exec, exec, s[12:13]
	s_waitcnt vmcnt(0)
	s_waitcnt vmcnt(0)

.LBB0_240:
	s_lshl_b32 s6, s45, 8
	s_add_u32 s6, s2, s6
	s_addc_u32 s7, s3, 0
	v_mov_b32_e32 v1, 0x1000
	v_mov_b32_e32 v3, 1
	global_atomic_add v3, v1, v3, s[6:7] offset:1024 sc0
	v_cvt_f32_u32_e32 v1, v2
	v_sub_u32_e32 v4, 0, v2
	v_rcp_iflag_f32_e32 v1, v1
	s_nop 0
	v_mul_f32_e32 v1, 0x4f7ffffe, v1
	v_cvt_u32_f32_e32 v1, v1
	v_mul_lo_u32 v4, v4, v1
	v_mul_hi_u32 v4, v1, v4
	v_add_u32_e32 v1, v1, v4
	s_waitcnt vmcnt(0)
	v_mul_hi_u32 v1, v3, v1
	v_mul_lo_u32 v4, v1, v2
	v_sub_u32_e32 v4, v3, v4
	v_add_u32_e32 v5, 1, v1
	v_cmp_ge_u32_e32 vcc, v4, v2
	v_add_u32_e32 v3, 1, v3
	s_nop 0
	v_cndmask_b32_e32 v1, v1, v5, vcc
	v_sub_u32_e32 v5, v4, v2
	v_cndmask_b32_e32 v4, v4, v5, vcc
	v_add_u32_e32 v5, 1, v1
	v_cmp_ge_u32_e32 vcc, v4, v2
	s_nop 1
	v_cndmask_b32_e32 v1, v1, v5, vcc
	v_mul_lo_u32 v4, v2, v1
	v_add_u32_e32 v2, v4, v2
	v_cmp_ne_u32_e32 vcc, v3, v2
	s_and_saveexec_b64 s[8:9], vcc
	s_xor_b64 s[8:9], exec, s[8:9]
	s_cbranch_execz .LBB0_254
	s_waitcnt lgkmcnt(0)
	v_mov_b32_e32 v0, 0x2000
	buffer_inv sc1
	global_load_dword v0, v0, s[6:7] offset:1024 sc1
	s_add_u32 s14, s6, 0x2400
	s_addc_u32 s15, s7, 0
	s_waitcnt vmcnt(0)
	v_cmp_eq_u32_e32 vcc, v0, v1
	s_and_saveexec_b64 s[10:11], vcc
	s_cbranch_execz .LBB0_253
	s_load_dwordx2 s[12:13], s[0:1], 0xc8
	s_mov_b32 s26, 1
	s_mov_b64 s[16:17], 0
	v_mov_b32_e32 v0, 0
	s_waitcnt lgkmcnt(0)
	s_add_u32 s12, s12, 0x4200
	s_addc_u32 s13, s13, 0
	s_branch .LBB0_244

.LBB0_253:
	s_or_b64 exec, exec, s[10:11]
	s_waitcnt vmcnt(0)
	s_waitcnt vmcnt(0)

.LBB0_476:
	v_readlane_b32 s6, v252, 15
	v_readlane_b32 s7, v252, 16
	v_cvt_f32_u32_e32 v0, v3
	v_sub_u32_e32 v5, 0, v3
	v_rcp_iflag_f32_e32 v0, v0
	s_nop 1
	global_atomic_add v4, v1, v236, s[6:7] sc0
	v_mul_f32_e32 v0, 0x4f7ffffe, v0
	v_cvt_u32_f32_e32 v0, v0
	v_mul_lo_u32 v5, v5, v0
	v_mul_hi_u32 v5, v0, v5
	v_add_u32_e32 v0, v0, v5
	s_waitcnt vmcnt(0)
	v_mul_hi_u32 v0, v4, v0
	v_mul_lo_u32 v5, v0, v3
	v_sub_u32_e32 v5, v4, v5
	v_add_u32_e32 v6, 1, v0
	v_cmp_ge_u32_e32 vcc, v5, v3
	v_add_u32_e32 v4, 1, v4
	s_nop 0
	v_cndmask_b32_e32 v0, v0, v6, vcc
	v_sub_u32_e32 v6, v5, v3
	v_cndmask_b32_e32 v5, v5, v6, vcc
	v_add_u32_e32 v6, 1, v0
	v_cmp_ge_u32_e32 vcc, v5, v3
	s_nop 1
	v_cndmask_b32_e32 v0, v0, v6, vcc
	v_mul_lo_u32 v5, v3, v0
	v_add_u32_e32 v3, v5, v3
	v_cmp_ne_u32_e32 vcc, v4, v3
	s_and_saveexec_b64 s[6:7], vcc
	s_xor_b64 s[6:7], exec, s[6:7]
	s_cbranch_execz .LBB0_490
	v_readlane_b32 s8, v252, 17
	v_readlane_b32 s9, v252, 18
	s_waitcnt lgkmcnt(0)
	s_nop 3
	buffer_inv sc1
	global_load_dword v2, v1, s[8:9] sc1
	s_waitcnt vmcnt(0)
	v_cmp_eq_u32_e32 vcc, v2, v0
	s_and_saveexec_b64 s[8:9], vcc
	s_cbranch_execz .LBB0_489
	s_mov_b32 s13, 1
	s_mov_b64 s[10:11], 0
	s_branch .LBB0_480

.LBB0_489:
	s_or_b64 exec, exec, s[8:9]
	s_waitcnt vmcnt(0)
	s_waitcnt vmcnt(0)

.LBB0_1037:
	v_readlane_b32 s4, v252, 15
	v_readlane_b32 s5, v252, 16
	v_cvt_f32_u32_e32 v0, v3
	v_sub_u32_e32 v5, 0, v3
	v_rcp_iflag_f32_e32 v0, v0
	s_nop 1
	global_atomic_add v4, v1, v236, s[4:5] sc0
	v_mul_f32_e32 v0, 0x4f7ffffe, v0
	v_cvt_u32_f32_e32 v0, v0
	v_mul_lo_u32 v5, v5, v0
	v_mul_hi_u32 v5, v0, v5
	v_add_u32_e32 v0, v0, v5
	s_waitcnt vmcnt(0)
	v_mul_hi_u32 v0, v4, v0
	v_mul_lo_u32 v5, v0, v3
	v_sub_u32_e32 v5, v4, v5
	v_add_u32_e32 v6, 1, v0
	v_cmp_ge_u32_e32 vcc, v5, v3
	v_add_u32_e32 v4, 1, v4
	s_nop 0
	v_cndmask_b32_e32 v0, v0, v6, vcc
	v_sub_u32_e32 v6, v5, v3
	v_cndmask_b32_e32 v5, v5, v6, vcc
	v_add_u32_e32 v6, 1, v0
	v_cmp_ge_u32_e32 vcc, v5, v3
	s_nop 1
	v_cndmask_b32_e32 v0, v0, v6, vcc
	v_mul_lo_u32 v5, v3, v0
	v_add_u32_e32 v3, v5, v3
	v_cmp_ne_u32_e32 vcc, v4, v3
	s_and_saveexec_b64 s[4:5], vcc
	s_xor_b64 s[4:5], exec, s[4:5]
	s_cbranch_execz .LBB0_1051
	v_readlane_b32 s6, v252, 17
	v_readlane_b32 s7, v252, 18
	s_waitcnt lgkmcnt(0)
	s_nop 3
	buffer_inv sc1
	global_load_dword v2, v1, s[6:7] sc1
	s_waitcnt vmcnt(0)
	v_cmp_eq_u32_e32 vcc, v2, v0
	s_and_saveexec_b64 s[6:7], vcc
	s_cbranch_execz .LBB0_1050
	s_mov_b32 s13, 1
	s_mov_b64 s[8:9], 0
	s_branch .LBB0_1041

.LBB0_1050:
	s_or_b64 exec, exec, s[6:7]
	s_waitcnt vmcnt(0)
	s_waitcnt vmcnt(0)

.LBB0_1498:
	v_readlane_b32 s0, v252, 15
	v_readlane_b32 s1, v252, 16
	v_cvt_f32_u32_e32 v0, v3
	v_sub_u32_e32 v5, 0, v3
	v_rcp_iflag_f32_e32 v0, v0
	s_nop 1
	global_atomic_add v4, v1, v236, s[0:1] sc0
	v_mul_f32_e32 v0, 0x4f7ffffe, v0
	v_cvt_u32_f32_e32 v0, v0
	v_mul_lo_u32 v5, v5, v0
	v_mul_hi_u32 v5, v0, v5
	v_add_u32_e32 v0, v0, v5
	s_waitcnt vmcnt(0)
	v_mul_hi_u32 v0, v4, v0
	v_mul_lo_u32 v5, v0, v3
	v_sub_u32_e32 v5, v4, v5
	v_add_u32_e32 v6, 1, v0
	v_cmp_ge_u32_e32 vcc, v5, v3
	v_add_u32_e32 v4, 1, v4
	s_nop 0
	v_cndmask_b32_e32 v0, v0, v6, vcc
	v_sub_u32_e32 v6, v5, v3
	v_cndmask_b32_e32 v5, v5, v6, vcc
	v_add_u32_e32 v6, 1, v0
	v_cmp_ge_u32_e32 vcc, v5, v3
	s_nop 1
	v_cndmask_b32_e32 v0, v0, v6, vcc
	v_mul_lo_u32 v5, v3, v0
	v_add_u32_e32 v3, v5, v3
	v_cmp_ne_u32_e32 vcc, v4, v3
	s_and_saveexec_b64 s[0:1], vcc
	s_xor_b64 s[6:7], exec, s[0:1]
	s_cbranch_execz .LBB0_1512
	v_readlane_b32 s0, v252, 17
	v_readlane_b32 s1, v252, 18
	s_waitcnt lgkmcnt(0)
	s_nop 3
	buffer_inv sc1
	global_load_dword v2, v1, s[0:1] sc1
	s_waitcnt vmcnt(0)
	v_cmp_eq_u32_e32 vcc, v2, v0
	s_and_saveexec_b64 s[8:9], vcc
	s_cbranch_execz .LBB0_1511
	s_mov_b32 s0, 1
	s_mov_b64 s[10:11], 0
	s_branch .LBB0_1502

.LBB0_1590:
	v_readlane_b32 s4, v252, 15
	v_readlane_b32 s5, v252, 16
	v_cvt_f32_u32_e32 v0, v3
	v_sub_u32_e32 v5, 0, v3
	v_rcp_iflag_f32_e32 v0, v0
	s_nop 1
	global_atomic_add v4, v1, v236, s[4:5] sc0
	v_mul_f32_e32 v0, 0x4f7ffffe, v0
	v_cvt_u32_f32_e32 v0, v0
	v_mul_lo_u32 v5, v5, v0
	v_mul_hi_u32 v5, v0, v5
	v_add_u32_e32 v0, v0, v5
	s_waitcnt vmcnt(0)
	v_mul_hi_u32 v0, v4, v0
	v_mul_lo_u32 v5, v0, v3
	v_sub_u32_e32 v5, v4, v5
	v_add_u32_e32 v6, 1, v0
	v_cmp_ge_u32_e32 vcc, v5, v3
	v_add_u32_e32 v4, 1, v4
	s_nop 0
	v_cndmask_b32_e32 v0, v0, v6, vcc
	v_sub_u32_e32 v6, v5, v3
	v_cndmask_b32_e32 v5, v5, v6, vcc
	v_add_u32_e32 v6, 1, v0
	v_cmp_ge_u32_e32 vcc, v5, v3
	s_nop 1
	v_cndmask_b32_e32 v0, v0, v6, vcc
	v_mul_lo_u32 v5, v3, v0
	v_add_u32_e32 v3, v5, v3
	v_cmp_ne_u32_e32 vcc, v4, v3
	s_and_saveexec_b64 s[4:5], vcc
	s_xor_b64 s[4:5], exec, s[4:5]
	s_cbranch_execz .LBB0_1604
	v_readlane_b32 s6, v252, 17
	v_readlane_b32 s7, v252, 18
	s_waitcnt lgkmcnt(0)
	s_nop 3
	buffer_inv sc1
	global_load_dword v2, v1, s[6:7] sc1
	s_waitcnt vmcnt(0)
	v_cmp_eq_u32_e32 vcc, v2, v0
	s_and_saveexec_b64 s[6:7], vcc
	s_cbranch_execz .LBB0_1603
	s_mov_b32 s26, 1
	s_mov_b64 s[8:9], 0
	s_branch .LBB0_1594

.LBB0_1694:
	v_readlane_b32 s6, v252, 15
	v_readlane_b32 s7, v252, 16
	v_cvt_f32_u32_e32 v0, v3
	v_sub_u32_e32 v5, 0, v3
	v_rcp_iflag_f32_e32 v0, v0
	s_nop 1
	global_atomic_add v4, v1, v236, s[6:7] sc0
	v_mul_f32_e32 v0, 0x4f7ffffe, v0
	v_cvt_u32_f32_e32 v0, v0
	v_mul_lo_u32 v5, v5, v0
	v_mul_hi_u32 v5, v0, v5
	v_add_u32_e32 v0, v0, v5
	s_waitcnt vmcnt(0)
	v_mul_hi_u32 v0, v4, v0
	v_mul_lo_u32 v5, v0, v3
	v_sub_u32_e32 v5, v4, v5
	v_add_u32_e32 v6, 1, v0
	v_cmp_ge_u32_e32 vcc, v5, v3
	v_add_u32_e32 v4, 1, v4
	s_nop 0
	v_cndmask_b32_e32 v0, v0, v6, vcc
	v_sub_u32_e32 v6, v5, v3
	v_cndmask_b32_e32 v5, v5, v6, vcc
	v_add_u32_e32 v6, 1, v0
	v_cmp_ge_u32_e32 vcc, v5, v3
	s_nop 1
	v_cndmask_b32_e32 v0, v0, v6, vcc
	v_mul_lo_u32 v5, v3, v0
	v_add_u32_e32 v3, v5, v3
	v_cmp_ne_u32_e32 vcc, v4, v3
	s_and_saveexec_b64 s[6:7], vcc
	s_xor_b64 s[6:7], exec, s[6:7]
	s_cbranch_execz .LBB0_1708
	v_readlane_b32 s8, v252, 17
	v_readlane_b32 s9, v252, 18
	s_waitcnt lgkmcnt(0)
	s_nop 3
	buffer_inv sc1
	global_load_dword v2, v1, s[8:9] sc1
	s_waitcnt vmcnt(0)
	v_cmp_eq_u32_e32 vcc, v2, v0
	s_and_saveexec_b64 s[8:9], vcc
	s_cbranch_execz .LBB0_1707
	s_mov_b32 s26, 1
	s_mov_b64 s[10:11], 0
	s_branch .LBB0_1698

.LBB0_2186:
	v_readlane_b32 s4, v252, 15
	v_readlane_b32 s5, v252, 16
	v_cvt_f32_u32_e32 v0, v3
	v_sub_u32_e32 v5, 0, v3
	v_rcp_iflag_f32_e32 v0, v0
	s_nop 1
	global_atomic_add v4, v1, v236, s[4:5] sc0
	v_mul_f32_e32 v0, 0x4f7ffffe, v0
	v_cvt_u32_f32_e32 v0, v0
	v_mul_lo_u32 v5, v5, v0
	v_mul_hi_u32 v5, v0, v5
	v_add_u32_e32 v0, v0, v5
	s_waitcnt vmcnt(0)
	v_mul_hi_u32 v0, v4, v0
	v_mul_lo_u32 v5, v0, v3
	v_sub_u32_e32 v5, v4, v5
	v_add_u32_e32 v6, 1, v0
	v_cmp_ge_u32_e32 vcc, v5, v3
	v_add_u32_e32 v4, 1, v4
	s_nop 0
	v_cndmask_b32_e32 v0, v0, v6, vcc
	v_sub_u32_e32 v6, v5, v3
	v_cndmask_b32_e32 v5, v5, v6, vcc
	v_add_u32_e32 v6, 1, v0
	v_cmp_ge_u32_e32 vcc, v5, v3
	s_nop 1
	v_cndmask_b32_e32 v0, v0, v6, vcc
	v_mul_lo_u32 v5, v3, v0
	v_add_u32_e32 v3, v5, v3
	v_cmp_ne_u32_e32 vcc, v4, v3
	s_and_saveexec_b64 s[4:5], vcc
	s_xor_b64 s[4:5], exec, s[4:5]
	s_cbranch_execz .LBB0_2200
	v_readlane_b32 s6, v252, 17
	v_readlane_b32 s7, v252, 18
	s_waitcnt lgkmcnt(0)
	s_nop 3
	buffer_inv sc1
	global_load_dword v2, v1, s[6:7] sc1
	s_waitcnt vmcnt(0)
	v_cmp_eq_u32_e32 vcc, v2, v0
	s_and_saveexec_b64 s[6:7], vcc
	s_cbranch_execz .LBB0_2199
	s_mov_b32 s23, 1
	s_mov_b64 s[8:9], 0
	s_branch .LBB0_2190
